# layer-1 PEER table rows converted in the shadow of layer-0 gemm2/gemm3 last partial round by the 224 idle workgroups instead of in the prologue
# speedup vs baseline: 1.0211x; 1.0039x over previous
.LBB0_34:
	s_andn2_b64 vcc, exec, s[22:23]
	s_cbranch_vccnz .LBB0_38
	s_add_i32 s48, s26, 0xffff5200
	s_and_b32 s49, s48, 0x7fff
	s_bitcmp1_b32 s49, 14
	s_cbranch_scc1 .LBB0_38
	s_cmpk_lt_u32 s48, 0x8000
	s_cselect_b64 s[22:23], -1, 0
	s_and_b64 s[24:25], s[22:23], exec
	s_cselect_b32 s25, s63, s65
	s_cselect_b32 s24, s62, s64
	s_lshl_b32 s50, s49, 13
	s_add_u32 s24, s24, s50
	s_addc_u32 s25, s25, 0
	v_lshl_add_u64 v[2:3], s[24:25], 0, v[36:37]
	global_load_dwordx4 v[30:33], v36, s[24:25] nt
	global_load_dwordx4 v[26:29], v36, s[24:25] offset:1024 nt
	global_load_dwordx4 v[22:25], v36, s[24:25] offset:2048 nt
	global_load_dwordx4 v[18:21], v36, s[24:25] offset:3072 nt
	v_add_co_u32_e32 v2, vcc, s42, v2
	v_and_b32_e32 v49, 64, v91
	s_nop 0
	v_addc_co_u32_e32 v3, vcc, 0, v3, vcc
	global_load_dwordx4 v[14:17], v[2:3], off nt
	global_load_dwordx4 v[10:13], v[2:3], off offset:1024 nt
	global_load_dwordx4 v[6:9], v[2:3], off offset:2048 nt
	s_nop 0
	global_load_dwordx4 v[2:5], v[2:3], off offset:3072 nt
	v_xor_b32_e32 v92, 1, v91
	v_add_u32_e32 v49, 64, v49
	v_cmp_lt_i32_e32 vcc, v92, v49
	s_waitcnt vmcnt(7)
	v_max_f32_e64 v93, |v33|, |v33|
	v_max_f32_e64 v94, |v32|, |v32|
	s_waitcnt vmcnt(6)
	v_max_f32_e64 v95, |v29|, |v29|
	v_max_f32_e64 v96, |v28|, |v28|
	s_waitcnt vmcnt(5)
	v_max_f32_e64 v97, |v25|, |v25|
	v_max_f32_e64 v98, |v24|, |v24|
	s_waitcnt vmcnt(4)
	v_max_f32_e64 v99, |v21|, |v21|
	v_max_f32_e64 v100, |v20|, |v20|
	v_max_f32_e32 v93, v94, v93
	v_max_f32_e32 v94, v96, v95
	v_max_f32_e32 v95, v98, v97
	v_max_f32_e32 v96, v100, v99
	v_max3_f32 v93, |v30|, |v31|, v93
	v_max3_f32 v94, |v26|, |v27|, v94
	s_waitcnt vmcnt(3)
	v_max_f32_e64 v97, |v17|, |v17|
	v_max_f32_e64 v98, |v16|, |v16|
	s_waitcnt vmcnt(2)
	v_max_f32_e64 v99, |v13|, |v13|
	v_max_f32_e64 v100, |v12|, |v12|
	v_max3_f32 v95, |v22|, |v23|, v95
	v_max3_f32 v96, |v18|, |v19|, v96
	s_waitcnt vmcnt(1)
	v_max_f32_e64 v101, |v9|, |v9|
	v_max_f32_e64 v102, |v8|, |v8|
	s_waitcnt vmcnt(0)
	v_max_f32_e64 v103, |v5|, |v5|
	v_max_f32_e64 v104, |v4|, |v4|
	v_max3_f32 v93, v93, 0, v94
	v_max_f32_e32 v94, v98, v97
	v_max_f32_e32 v97, v100, v99
	v_max_f32_e32 v98, v102, v101
	v_max_f32_e32 v99, v104, v103
	v_max3_f32 v93, v93, v95, v96
	v_max3_f32 v94, |v14|, |v15|, v94
	v_max3_f32 v95, |v10|, |v11|, v97
	v_cndmask_b32_e32 v92, v91, v92, vcc
	v_max3_f32 v96, |v6|, |v7|, v98
	v_max3_f32 v97, |v2|, |v3|, v99
	v_max3_f32 v93, v93, v94, v95
	v_lshlrev_b32_e32 v92, 2, v92
	v_max3_f32 v93, v93, v96, v97
	ds_bpermute_b32 v92, v92, v93
	v_xor_b32_e32 v94, 2, v91
	v_cmp_lt_i32_e32 vcc, v94, v49
	s_waitcnt lgkmcnt(0)
	v_max_f32_e32 v92, v92, v92
	v_cndmask_b32_e32 v94, v91, v94, vcc
	v_lshlrev_b32_e32 v94, 2, v94
	v_max_f32_e32 v92, v93, v92
	ds_bpermute_b32 v93, v94, v92
	v_xor_b32_e32 v94, 4, v91
	v_cmp_lt_i32_e32 vcc, v94, v49
	s_waitcnt lgkmcnt(0)
	v_max_f32_e32 v93, v93, v93
	v_cndmask_b32_e32 v94, v91, v94, vcc
	v_lshlrev_b32_e32 v94, 2, v94
	v_max_f32_e32 v92, v92, v93
	ds_bpermute_b32 v93, v94, v92
	v_xor_b32_e32 v94, 8, v91
	v_cmp_lt_i32_e32 vcc, v94, v49
	s_waitcnt lgkmcnt(0)
	v_max_f32_e32 v93, v93, v93
	v_cndmask_b32_e32 v94, v91, v94, vcc
	v_lshlrev_b32_e32 v94, 2, v94
	v_max_f32_e32 v92, v92, v93
	ds_bpermute_b32 v93, v94, v92
	v_xor_b32_e32 v94, 16, v91
	v_cmp_lt_i32_e32 vcc, v94, v49
	s_waitcnt lgkmcnt(0)
	v_max_f32_e32 v93, v93, v93
	v_cndmask_b32_e32 v94, v91, v94, vcc
	v_lshlrev_b32_e32 v94, 2, v94
	v_max_f32_e32 v92, v92, v93
	ds_bpermute_b32 v93, v94, v92
	v_xor_b32_e32 v94, 32, v91
	v_cmp_lt_i32_e32 vcc, v94, v49
	s_waitcnt lgkmcnt(0)
	v_max_f32_e32 v93, v93, v93
	v_cndmask_b32_e32 v49, v91, v94, vcc
	v_max_f32_e32 v92, v92, v93
	v_lshlrev_b32_e32 v49, 2, v49
	ds_bpermute_b32 v49, v49, v92
	s_waitcnt lgkmcnt(0)
	v_max_f32_e32 v49, v49, v49
	v_max_f32_e32 v49, v92, v49
	s_and_saveexec_b64 s[24:25], s[0:1]
	s_cbranch_execz .LBB0_37
	s_and_b64 s[50:51], s[22:23], exec
	s_mov_b32 s50, 0x12a00000
	s_cselect_b32 s50, s50, 0x12a20000
	s_add_u32 s50, s70, s50
	s_addc_u32 s51, s71, 0
	s_lshl_b32 s49, s49, 2
	v_mul_f32_e32 v92, 0x3b124925, v49
	v_mov_b32_e32 v93, s49
	global_store_dword v93, v92, s[50:51]

.LBB0_611:
	v_readlane_b32 s4, v255, 36
	v_readlane_b32 s8, v252, 0
	s_add_i32 s5, s4, 7
	v_readlane_b32 s9, v252, 1
	s_cmp_ge_i32 s5, s9
	v_readlane_b32 s10, v252, 2
	v_readlane_b32 s11, v252, 3
	s_cbranch_scc1 .LBB0_661
	v_readlane_b32 s4, v255, 34
	s_nop 0
	s_cmp_lg_u32 s4, 0
	s_cbranch_scc1 .Ldfu_done
	s_cmp_gt_u32 s82, 32
	s_cselect_b32 s11, 32, 0
	s_cmp_lt_u32 s2, s11
	s_cbranch_scc1 .Ldfu_done
	s_sub_u32 s10, s82, s11
	s_lshl_b32 s10, s10, 3
	s_sub_u32 s4, s2, s11
	s_lshl_b32 s4, s4, 3
	v_readfirstlane_b32 s11, v0
	s_lshr_b32 s11, s11, 6
	s_add_u32 s4, s4, s11
	s_cmp_ge_u32 s4, 0x4000
	s_cbranch_scc1 .Ldfu_done
	v_readlane_b32 s6, v252, 4
	v_readlane_b32 s7, v252, 5
	s_nop 0
	s_sub_u32 s6, s6, 0x38
	s_subb_u32 s7, s7, 0
	s_load_dwordx2 s[8:9], s[6:7], 0x0
	s_load_dwordx2 s[6:7], s[6:7], 0x20
	v_and_b32_e32 v6, 63, v0
	v_lshlrev_b32_e32 v7, 4, v6
	v_lshrrev_b32_e32 v56, 5, v6
	v_and_b32_e32 v57, 31, v6
	v_lshlrev_b32_e32 v56, 21, v56
	v_lshl_add_u32 v56, v57, 2, v56
	v_add_u32_e32 v56, 0xca00000, v56
	s_mov_b64 exec, -1
	s_waitcnt lgkmcnt(0)
	s_add_u32 s11, s4, 0x4000
	s_lshl_b32 s11, s11, 13
	v_add_u32_e32 v40, s11, v7
	v_add_u32_e32 v41, 0x1000, v40
	global_load_dwordx4 v[8:11], v40, s[8:9] nt
	global_load_dwordx4 v[12:15], v40, s[8:9] offset:1024 nt
	global_load_dwordx4 v[16:19], v40, s[8:9] offset:2048 nt
	global_load_dwordx4 v[20:23], v40, s[8:9] offset:3072 nt
	global_load_dwordx4 v[24:27], v41, s[8:9] nt
	global_load_dwordx4 v[28:31], v41, s[8:9] offset:1024 nt
	global_load_dwordx4 v[32:35], v41, s[8:9] offset:2048 nt
	global_load_dwordx4 v[36:39], v41, s[8:9] offset:3072 nt
.Ldfu_loop:
	s_add_u32 s11, s4, s10
	s_min_u32 s11, s11, 0x3fff
	s_mov_b32 s101, s11
	s_add_u32 s11, s101, 0x4000
	s_lshl_b32 s11, s11, 13
	v_add_u32_e32 v40, s11, v7
	v_add_u32_e32 v41, 0x1000, v40
	global_load_dwordx4 v[76:79], v40, s[8:9] nt
	global_load_dwordx4 v[80:83], v40, s[8:9] offset:1024 nt
	global_load_dwordx4 v[84:87], v40, s[8:9] offset:2048 nt
	global_load_dwordx4 v[88:91], v40, s[8:9] offset:3072 nt
	global_load_dwordx4 v[92:95], v41, s[8:9] nt
	global_load_dwordx4 v[96:99], v41, s[8:9] offset:1024 nt
	global_load_dwordx4 v[100:103], v41, s[8:9] offset:2048 nt
	global_load_dwordx4 v[104:107], v41, s[8:9] offset:3072 nt
	s_waitcnt vmcnt(8)
	v_max3_f32 v42, |v8|, |v9|, |v10|
	v_max3_f32 v43, |v12|, |v13|, |v14|
	v_max3_f32 v44, |v16|, |v17|, |v18|
	v_max3_f32 v45, |v20|, |v21|, |v22|
	v_max3_f32 v46, |v24|, |v25|, |v26|
	v_max3_f32 v47, |v28|, |v29|, |v30|
	v_max3_f32 v48, |v32|, |v33|, |v34|
	v_max3_f32 v49, |v36|, |v37|, |v38|
	v_max_f32_e64 v42, v42, |v11|
	v_max_f32_e64 v43, v43, |v15|
	v_max_f32_e64 v44, v44, |v19|
	v_max_f32_e64 v45, v45, |v23|
	v_max_f32_e64 v46, v46, |v27|
	v_max_f32_e64 v47, v47, |v31|
	v_max_f32_e64 v48, v48, |v35|
	v_max_f32_e64 v49, v49, |v39|
	v_max3_f32 v42, v42, v43, v44
	v_max3_f32 v45, v45, v46, v47
	v_max3_f32 v42, v42, v45, v48
	v_max_f32_e32 v42, v42, v49
	s_nop 1
	v_max_f32_dpp v43, v42, v42 quad_perm:[1,0,3,2] row_mask:0xf bank_mask:0xf bound_ctrl:1
	s_nop 1
	v_max_f32_dpp v42, v43, v43 quad_perm:[2,3,0,1] row_mask:0xf bank_mask:0xf bound_ctrl:1
	s_nop 1
	v_max_f32_dpp v43, v42, v42 row_half_mirror row_mask:0xf bank_mask:0xf bound_ctrl:1
	s_nop 1
	v_max_f32_dpp v42, v43, v43 row_mirror row_mask:0xf bank_mask:0xf bound_ctrl:1
	s_nop 1
	v_mov_b32_e32 v43, v42
	s_nop 1
	v_permlane16_swap_b32_e32 v42, v43
	v_max_f32_e32 v42, v42, v43
	v_mov_b32_e32 v43, v42
	s_nop 1
	v_permlane32_swap_b32_e32 v42, v43
	v_max_f32_e32 v49, v42, v43
	v_mul_f32_e32 v44, 0x3b124925, v49
	s_add_u32 s11, s4, 0x4000
	s_lshl_b32 s11, s11, 2
	s_add_u32 s11, s11, 0x12a00000
	v_mov_b32_e32 v45, s11
	s_mov_b64 exec, 1
	global_store_dword v45, v44, s[6:7]
	s_mov_b64 exec, -1
	v_mov_b32_e32 v46, 0x43e00000
	v_div_scale_f32 v42, s[100:101], v49, v49, v46
	v_rcp_f32_e32 v43, v42
	s_nop 0
	v_fma_f32 v44, -v42, v43, 1.0
	v_fmac_f32_e32 v43, v44, v43
	v_div_scale_f32 v44, vcc, v46, v49, v46
	v_mul_f32_e32 v45, v44, v43
	v_fma_f32 v47, -v42, v45, v44
	v_fmac_f32_e32 v45, v47, v43
	v_fma_f32 v42, -v42, v45, v44
	s_nop 1
	v_div_fmas_f32 v42, v42, v43, v45
	v_div_fixup_f32 v42, v42, v49, v46
	v_cmp_lt_f32_e32 vcc, 0, v49
	s_nop 1
	v_cndmask_b32_e32 v48, 0, v42, vcc
	v_mul_f32_e32 v8, v8, v48
	v_mul_f32_e32 v9, v9, v48
	v_mul_f32_e32 v10, v10, v48
	v_mul_f32_e32 v11, v11, v48
	v_mul_f32_e32 v12, v12, v48
	v_mul_f32_e32 v13, v13, v48
	v_mul_f32_e32 v14, v14, v48
	v_mul_f32_e32 v15, v15, v48
	v_mul_f32_e32 v16, v16, v48
	v_mul_f32_e32 v17, v17, v48
	v_mul_f32_e32 v18, v18, v48
	v_mul_f32_e32 v19, v19, v48
	v_mul_f32_e32 v20, v20, v48
	v_mul_f32_e32 v21, v21, v48
	v_mul_f32_e32 v22, v22, v48
	v_mul_f32_e32 v23, v23, v48
	v_mul_f32_e32 v24, v24, v48
	v_mul_f32_e32 v25, v25, v48
	v_mul_f32_e32 v26, v26, v48
	v_mul_f32_e32 v27, v27, v48
	v_mul_f32_e32 v28, v28, v48
	v_mul_f32_e32 v29, v29, v48
	v_mul_f32_e32 v30, v30, v48
	v_mul_f32_e32 v31, v31, v48
	v_mul_f32_e32 v32, v32, v48
	v_mul_f32_e32 v33, v33, v48
	v_mul_f32_e32 v34, v34, v48
	v_mul_f32_e32 v35, v35, v48
	v_mul_f32_e32 v36, v36, v48
	v_mul_f32_e32 v37, v37, v48
	v_mul_f32_e32 v38, v38, v48
	v_mul_f32_e32 v39, v39, v48
	v_mov_b32_e32 v58, 0
	v_mov_b32_e32 v59, 0
	v_mov_b32_e32 v60, 0
	v_mov_b32_e32 v61, 0
	v_mov_b32_e32 v62, 0
	v_mov_b32_e32 v63, 0
	v_mov_b32_e32 v64, 0
	v_mov_b32_e32 v65, 0
	v_cvt_pk_fp8_f32 v58, v8, v9
	v_cvt_pk_fp8_f32 v59, v12, v13
	v_cvt_pk_fp8_f32 v60, v16, v17
	v_cvt_pk_fp8_f32 v61, v20, v21
	v_cvt_pk_fp8_f32 v62, v24, v25
	v_cvt_pk_fp8_f32 v63, v28, v29
	v_cvt_pk_fp8_f32 v64, v32, v33
	v_cvt_pk_fp8_f32 v65, v36, v37
	v_cvt_pk_fp8_f32 v58, v10, v11 op_sel:[0,0,1]
	v_cvt_pk_fp8_f32 v59, v14, v15 op_sel:[0,0,1]
	v_cvt_pk_fp8_f32 v60, v18, v19 op_sel:[0,0,1]
	v_cvt_pk_fp8_f32 v61, v22, v23 op_sel:[0,0,1]
	v_cvt_pk_fp8_f32 v62, v26, v27 op_sel:[0,0,1]
	v_cvt_pk_fp8_f32 v63, v30, v31 op_sel:[0,0,1]
	v_cvt_pk_fp8_f32 v64, v34, v35 op_sel:[0,0,1]
	v_cvt_pk_fp8_f32 v65, v38, v39 op_sel:[0,0,1]
	s_lshl_b32 s11, s4, 7
	v_add_u32_e32 v66, s11, v56
	v_add_u32_e32 v67, 0x400000, v66
	v_add_u32_e32 v68, 0x800000, v66
	v_add_u32_e32 v69, 0xc00000, v66
	v_add_u32_e32 v70, 0x1000000, v66
	v_add_u32_e32 v71, 0x1400000, v66
	v_add_u32_e32 v72, 0x1800000, v66
	v_add_u32_e32 v73, 0x1c00000, v66
	global_store_dword v66, v58, s[6:7]
	global_store_dword v67, v59, s[6:7]
	global_store_dword v68, v60, s[6:7]
	global_store_dword v69, v61, s[6:7]
	global_store_dword v70, v62, s[6:7]
	global_store_dword v71, v63, s[6:7]
	global_store_dword v72, v64, s[6:7]
	global_store_dword v73, v65, s[6:7]
	s_add_u32 s4, s4, s10
	s_cmp_ge_u32 s4, 0x4000
	s_cbranch_scc1 .Ldfu_done
	s_add_u32 s11, s4, s10
	s_min_u32 s11, s11, 0x3fff
	s_mov_b32 s101, s11
	s_add_u32 s11, s101, 0x4000
	s_lshl_b32 s11, s11, 13
	v_add_u32_e32 v40, s11, v7
	v_add_u32_e32 v41, 0x1000, v40
	global_load_dwordx4 v[8:11], v40, s[8:9] nt
	global_load_dwordx4 v[12:15], v40, s[8:9] offset:1024 nt
	global_load_dwordx4 v[16:19], v40, s[8:9] offset:2048 nt
	global_load_dwordx4 v[20:23], v40, s[8:9] offset:3072 nt
	global_load_dwordx4 v[24:27], v41, s[8:9] nt
	global_load_dwordx4 v[28:31], v41, s[8:9] offset:1024 nt
	global_load_dwordx4 v[32:35], v41, s[8:9] offset:2048 nt
	global_load_dwordx4 v[36:39], v41, s[8:9] offset:3072 nt
	s_waitcnt vmcnt(8)
	v_max3_f32 v42, |v76|, |v77|, |v78|
	v_max3_f32 v43, |v80|, |v81|, |v82|
	v_max3_f32 v44, |v84|, |v85|, |v86|
	v_max3_f32 v45, |v88|, |v89|, |v90|
	v_max3_f32 v46, |v92|, |v93|, |v94|
	v_max3_f32 v47, |v96|, |v97|, |v98|
	v_max3_f32 v48, |v100|, |v101|, |v102|
	v_max3_f32 v49, |v104|, |v105|, |v106|
	v_max_f32_e64 v42, v42, |v79|
	v_max_f32_e64 v43, v43, |v83|
	v_max_f32_e64 v44, v44, |v87|
	v_max_f32_e64 v45, v45, |v91|
	v_max_f32_e64 v46, v46, |v95|
	v_max_f32_e64 v47, v47, |v99|
	v_max_f32_e64 v48, v48, |v103|
	v_max_f32_e64 v49, v49, |v107|
	v_max3_f32 v42, v42, v43, v44
	v_max3_f32 v45, v45, v46, v47
	v_max3_f32 v42, v42, v45, v48
	v_max_f32_e32 v42, v42, v49
	s_nop 1
	v_max_f32_dpp v43, v42, v42 quad_perm:[1,0,3,2] row_mask:0xf bank_mask:0xf bound_ctrl:1
	s_nop 1
	v_max_f32_dpp v42, v43, v43 quad_perm:[2,3,0,1] row_mask:0xf bank_mask:0xf bound_ctrl:1
	s_nop 1
	v_max_f32_dpp v43, v42, v42 row_half_mirror row_mask:0xf bank_mask:0xf bound_ctrl:1
	s_nop 1
	v_max_f32_dpp v42, v43, v43 row_mirror row_mask:0xf bank_mask:0xf bound_ctrl:1
	s_nop 1
	v_mov_b32_e32 v43, v42
	s_nop 1
	v_permlane16_swap_b32_e32 v42, v43
	v_max_f32_e32 v42, v42, v43
	v_mov_b32_e32 v43, v42
	s_nop 1
	v_permlane32_swap_b32_e32 v42, v43
	v_max_f32_e32 v49, v42, v43
	v_mul_f32_e32 v44, 0x3b124925, v49
	s_add_u32 s11, s4, 0x4000
	s_lshl_b32 s11, s11, 2
	s_add_u32 s11, s11, 0x12a00000
	v_mov_b32_e32 v45, s11
	s_mov_b64 exec, 1
	global_store_dword v45, v44, s[6:7]
	s_mov_b64 exec, -1
	v_mov_b32_e32 v46, 0x43e00000
	v_div_scale_f32 v42, s[100:101], v49, v49, v46
	v_rcp_f32_e32 v43, v42
	s_nop 0
	v_fma_f32 v44, -v42, v43, 1.0
	v_fmac_f32_e32 v43, v44, v43
	v_div_scale_f32 v44, vcc, v46, v49, v46
	v_mul_f32_e32 v45, v44, v43
	v_fma_f32 v47, -v42, v45, v44
	v_fmac_f32_e32 v45, v47, v43
	v_fma_f32 v42, -v42, v45, v44
	s_nop 1
	v_div_fmas_f32 v42, v42, v43, v45
	v_div_fixup_f32 v42, v42, v49, v46
	v_cmp_lt_f32_e32 vcc, 0, v49
	s_nop 1
	v_cndmask_b32_e32 v48, 0, v42, vcc
	v_mul_f32_e32 v76, v76, v48
	v_mul_f32_e32 v77, v77, v48
	v_mul_f32_e32 v78, v78, v48
	v_mul_f32_e32 v79, v79, v48
	v_mul_f32_e32 v80, v80, v48
	v_mul_f32_e32 v81, v81, v48
	v_mul_f32_e32 v82, v82, v48
	v_mul_f32_e32 v83, v83, v48
	v_mul_f32_e32 v84, v84, v48
	v_mul_f32_e32 v85, v85, v48
	v_mul_f32_e32 v86, v86, v48
	v_mul_f32_e32 v87, v87, v48
	v_mul_f32_e32 v88, v88, v48
	v_mul_f32_e32 v89, v89, v48
	v_mul_f32_e32 v90, v90, v48
	v_mul_f32_e32 v91, v91, v48
	v_mul_f32_e32 v92, v92, v48
	v_mul_f32_e32 v93, v93, v48
	v_mul_f32_e32 v94, v94, v48
	v_mul_f32_e32 v95, v95, v48
	v_mul_f32_e32 v96, v96, v48
	v_mul_f32_e32 v97, v97, v48
	v_mul_f32_e32 v98, v98, v48
	v_mul_f32_e32 v99, v99, v48
	v_mul_f32_e32 v100, v100, v48
	v_mul_f32_e32 v101, v101, v48
	v_mul_f32_e32 v102, v102, v48
	v_mul_f32_e32 v103, v103, v48
	v_mul_f32_e32 v104, v104, v48
	v_mul_f32_e32 v105, v105, v48
	v_mul_f32_e32 v106, v106, v48
	v_mul_f32_e32 v107, v107, v48
	v_mov_b32_e32 v58, 0
	v_mov_b32_e32 v59, 0
	v_mov_b32_e32 v60, 0
	v_mov_b32_e32 v61, 0
	v_mov_b32_e32 v62, 0
	v_mov_b32_e32 v63, 0
	v_mov_b32_e32 v64, 0
	v_mov_b32_e32 v65, 0
	v_cvt_pk_fp8_f32 v58, v76, v77
	v_cvt_pk_fp8_f32 v59, v80, v81
	v_cvt_pk_fp8_f32 v60, v84, v85
	v_cvt_pk_fp8_f32 v61, v88, v89
	v_cvt_pk_fp8_f32 v62, v92, v93
	v_cvt_pk_fp8_f32 v63, v96, v97
	v_cvt_pk_fp8_f32 v64, v100, v101
	v_cvt_pk_fp8_f32 v65, v104, v105
	v_cvt_pk_fp8_f32 v58, v78, v79 op_sel:[0,0,1]
	v_cvt_pk_fp8_f32 v59, v82, v83 op_sel:[0,0,1]
	v_cvt_pk_fp8_f32 v60, v86, v87 op_sel:[0,0,1]
	v_cvt_pk_fp8_f32 v61, v90, v91 op_sel:[0,0,1]
	v_cvt_pk_fp8_f32 v62, v94, v95 op_sel:[0,0,1]
	v_cvt_pk_fp8_f32 v63, v98, v99 op_sel:[0,0,1]
	v_cvt_pk_fp8_f32 v64, v102, v103 op_sel:[0,0,1]
	v_cvt_pk_fp8_f32 v65, v106, v107 op_sel:[0,0,1]
	s_lshl_b32 s11, s4, 7
	v_add_u32_e32 v66, s11, v56
	v_add_u32_e32 v67, 0x400000, v66
	v_add_u32_e32 v68, 0x800000, v66
	v_add_u32_e32 v69, 0xc00000, v66
	v_add_u32_e32 v70, 0x1000000, v66
	v_add_u32_e32 v71, 0x1400000, v66
	v_add_u32_e32 v72, 0x1800000, v66
	v_add_u32_e32 v73, 0x1c00000, v66
	global_store_dword v66, v58, s[6:7]
	global_store_dword v67, v59, s[6:7]
	global_store_dword v68, v60, s[6:7]
	global_store_dword v69, v61, s[6:7]
	global_store_dword v70, v62, s[6:7]
	global_store_dword v71, v63, s[6:7]
	global_store_dword v72, v64, s[6:7]
	global_store_dword v73, v65, s[6:7]
	s_add_u32 s4, s4, s10
	s_cmp_ge_u32 s4, 0x4000
	s_cbranch_scc1 .Ldfu_done
	s_branch .Ldfu_loop
.Ldfu_done:
	v_readlane_b32 s8, v252, 0
	v_readlane_b32 s9, v252, 1
	v_readlane_b32 s10, v252, 2
	v_readlane_b32 s11, v252, 3
.Ldfu_end:
	v_readlane_b32 s4, v255, 36
	s_waitcnt vmcnt(0)
	s_waitcnt lgkmcnt(0)
	s_barrier
	s_mov_b64 s[6:7], exec
	v_readlane_b32 s8, v254, 52
	v_readlane_b32 s9, v254, 53
	s_and_b64 s[8:9], s[6:7], s[8:9]
	s_mov_b64 exec, s[8:9]
	s_cbranch_execz .LBB0_660
	v_readlane_b32 s8, v252, 42
	s_waitcnt vmcnt(0) expcnt(0) lgkmcnt(0)
	s_nop 0
	v_mov_b32_e32 v2, s8
	ds_read_b32 v5, v2
	ds_read_b32 v2, v2 offset:4
	s_waitcnt lgkmcnt(1)
	v_cmp_ne_u32_e32 vcc, 0, v5
	s_cbranch_vccnz .LBB0_628
	v_readlane_b32 s10, v252, 4
	v_readlane_b32 s11, v252, 5
	s_load_dwordx2 s[8:9], s[10:11], 0x4
	s_mov_b32 s15, 1
	s_waitcnt lgkmcnt(0)
	s_mul_i32 s14, s8, s82
	s_mul_i32 s14, s14, s9
	s_branch .LBB0_616

.LBB0_709:
	v_readlane_b32 s4, v255, 36
	v_readlane_b32 s8, v252, 0
	s_add_i32 s5, s4, 8
	v_readlane_b32 s9, v252, 1
	s_cmp_ge_i32 s5, s9
	v_readlane_b32 s10, v252, 2
	v_readlane_b32 s11, v252, 3
	s_cbranch_scc1 .LBB0_721
	v_readlane_b32 s4, v255, 34
	s_nop 0
	s_cmp_lg_u32 s4, 0
	s_cbranch_scc1 .Ldfv_done
	s_cmp_gt_u32 s82, 32
	s_cselect_b32 s11, 32, 0
	s_cmp_lt_u32 s2, s11
	s_cbranch_scc1 .Ldfv_done
	s_sub_u32 s10, s82, s11
	s_lshl_b32 s10, s10, 3
	s_sub_u32 s4, s2, s11
	s_lshl_b32 s4, s4, 3
	v_readfirstlane_b32 s11, v0
	s_lshr_b32 s11, s11, 6
	s_add_u32 s4, s4, s11
	s_cmp_ge_u32 s4, 0x4000
	s_cbranch_scc1 .Ldfv_done
	v_readlane_b32 s6, v252, 4
	v_readlane_b32 s7, v252, 5
	s_nop 0
	s_sub_u32 s6, s6, 0x38
	s_subb_u32 s7, s7, 0
	s_load_dwordx2 s[8:9], s[6:7], 0x8
	s_load_dwordx2 s[6:7], s[6:7], 0x20
	v_and_b32_e32 v6, 63, v0
	v_lshlrev_b32_e32 v7, 4, v6
	v_lshrrev_b32_e32 v56, 5, v6
	v_and_b32_e32 v57, 31, v6
	v_lshlrev_b32_e32 v56, 21, v56
	v_lshl_add_u32 v56, v57, 2, v56
	v_add_u32_e32 v56, 0x10a00000, v56
	s_mov_b64 exec, -1
	s_waitcnt lgkmcnt(0)
	s_add_u32 s11, s4, 0x4000
	s_lshl_b32 s11, s11, 13
	v_add_u32_e32 v40, s11, v7
	v_add_u32_e32 v41, 0x1000, v40
	global_load_dwordx4 v[8:11], v40, s[8:9] nt
	global_load_dwordx4 v[12:15], v40, s[8:9] offset:1024 nt
	global_load_dwordx4 v[16:19], v40, s[8:9] offset:2048 nt
	global_load_dwordx4 v[20:23], v40, s[8:9] offset:3072 nt
	global_load_dwordx4 v[24:27], v41, s[8:9] nt
	global_load_dwordx4 v[28:31], v41, s[8:9] offset:1024 nt
	global_load_dwordx4 v[32:35], v41, s[8:9] offset:2048 nt
	global_load_dwordx4 v[36:39], v41, s[8:9] offset:3072 nt
.Ldfv_loop:
	s_add_u32 s11, s4, s10
	s_min_u32 s11, s11, 0x3fff
	s_mov_b32 s101, s11
	s_add_u32 s11, s101, 0x4000
	s_lshl_b32 s11, s11, 13
	v_add_u32_e32 v40, s11, v7
	v_add_u32_e32 v41, 0x1000, v40
	global_load_dwordx4 v[76:79], v40, s[8:9] nt
	global_load_dwordx4 v[80:83], v40, s[8:9] offset:1024 nt
	global_load_dwordx4 v[84:87], v40, s[8:9] offset:2048 nt
	global_load_dwordx4 v[88:91], v40, s[8:9] offset:3072 nt
	global_load_dwordx4 v[92:95], v41, s[8:9] nt
	global_load_dwordx4 v[96:99], v41, s[8:9] offset:1024 nt
	global_load_dwordx4 v[100:103], v41, s[8:9] offset:2048 nt
	global_load_dwordx4 v[104:107], v41, s[8:9] offset:3072 nt
	s_waitcnt vmcnt(8)
	v_max3_f32 v42, |v8|, |v9|, |v10|
	v_max3_f32 v43, |v12|, |v13|, |v14|
	v_max3_f32 v44, |v16|, |v17|, |v18|
	v_max3_f32 v45, |v20|, |v21|, |v22|
	v_max3_f32 v46, |v24|, |v25|, |v26|
	v_max3_f32 v47, |v28|, |v29|, |v30|
	v_max3_f32 v48, |v32|, |v33|, |v34|
	v_max3_f32 v49, |v36|, |v37|, |v38|
	v_max_f32_e64 v42, v42, |v11|
	v_max_f32_e64 v43, v43, |v15|
	v_max_f32_e64 v44, v44, |v19|
	v_max_f32_e64 v45, v45, |v23|
	v_max_f32_e64 v46, v46, |v27|
	v_max_f32_e64 v47, v47, |v31|
	v_max_f32_e64 v48, v48, |v35|
	v_max_f32_e64 v49, v49, |v39|
	v_max3_f32 v42, v42, v43, v44
	v_max3_f32 v45, v45, v46, v47
	v_max3_f32 v42, v42, v45, v48
	v_max_f32_e32 v42, v42, v49
	s_nop 1
	v_max_f32_dpp v43, v42, v42 quad_perm:[1,0,3,2] row_mask:0xf bank_mask:0xf bound_ctrl:1
	s_nop 1
	v_max_f32_dpp v42, v43, v43 quad_perm:[2,3,0,1] row_mask:0xf bank_mask:0xf bound_ctrl:1
	s_nop 1
	v_max_f32_dpp v43, v42, v42 row_half_mirror row_mask:0xf bank_mask:0xf bound_ctrl:1
	s_nop 1
	v_max_f32_dpp v42, v43, v43 row_mirror row_mask:0xf bank_mask:0xf bound_ctrl:1
	s_nop 1
	v_mov_b32_e32 v43, v42
	s_nop 1
	v_permlane16_swap_b32_e32 v42, v43
	v_max_f32_e32 v42, v42, v43
	v_mov_b32_e32 v43, v42
	s_nop 1
	v_permlane32_swap_b32_e32 v42, v43
	v_max_f32_e32 v49, v42, v43
	v_mul_f32_e32 v44, 0x3b124925, v49
	s_add_u32 s11, s4, 0x4000
	s_lshl_b32 s11, s11, 2
	s_add_u32 s11, s11, 0x12a20000
	v_mov_b32_e32 v45, s11
	s_mov_b64 exec, 1
	global_store_dword v45, v44, s[6:7]
	s_mov_b64 exec, -1
	v_mov_b32_e32 v46, 0x43e00000
	v_div_scale_f32 v42, s[100:101], v49, v49, v46
	v_rcp_f32_e32 v43, v42
	s_nop 0
	v_fma_f32 v44, -v42, v43, 1.0
	v_fmac_f32_e32 v43, v44, v43
	v_div_scale_f32 v44, vcc, v46, v49, v46
	v_mul_f32_e32 v45, v44, v43
	v_fma_f32 v47, -v42, v45, v44
	v_fmac_f32_e32 v45, v47, v43
	v_fma_f32 v42, -v42, v45, v44
	s_nop 1
	v_div_fmas_f32 v42, v42, v43, v45
	v_div_fixup_f32 v42, v42, v49, v46
	v_cmp_lt_f32_e32 vcc, 0, v49
	s_nop 1
	v_cndmask_b32_e32 v48, 0, v42, vcc
	v_mul_f32_e32 v8, v8, v48
	v_mul_f32_e32 v9, v9, v48
	v_mul_f32_e32 v10, v10, v48
	v_mul_f32_e32 v11, v11, v48
	v_mul_f32_e32 v12, v12, v48
	v_mul_f32_e32 v13, v13, v48
	v_mul_f32_e32 v14, v14, v48
	v_mul_f32_e32 v15, v15, v48
	v_mul_f32_e32 v16, v16, v48
	v_mul_f32_e32 v17, v17, v48
	v_mul_f32_e32 v18, v18, v48
	v_mul_f32_e32 v19, v19, v48
	v_mul_f32_e32 v20, v20, v48
	v_mul_f32_e32 v21, v21, v48
	v_mul_f32_e32 v22, v22, v48
	v_mul_f32_e32 v23, v23, v48
	v_mul_f32_e32 v24, v24, v48
	v_mul_f32_e32 v25, v25, v48
	v_mul_f32_e32 v26, v26, v48
	v_mul_f32_e32 v27, v27, v48
	v_mul_f32_e32 v28, v28, v48
	v_mul_f32_e32 v29, v29, v48
	v_mul_f32_e32 v30, v30, v48
	v_mul_f32_e32 v31, v31, v48
	v_mul_f32_e32 v32, v32, v48
	v_mul_f32_e32 v33, v33, v48
	v_mul_f32_e32 v34, v34, v48
	v_mul_f32_e32 v35, v35, v48
	v_mul_f32_e32 v36, v36, v48
	v_mul_f32_e32 v37, v37, v48
	v_mul_f32_e32 v38, v38, v48
	v_mul_f32_e32 v39, v39, v48
	v_mov_b32_e32 v58, 0
	v_mov_b32_e32 v59, 0
	v_mov_b32_e32 v60, 0
	v_mov_b32_e32 v61, 0
	v_mov_b32_e32 v62, 0
	v_mov_b32_e32 v63, 0
	v_mov_b32_e32 v64, 0
	v_mov_b32_e32 v65, 0
	v_cvt_pk_fp8_f32 v58, v8, v9
	v_cvt_pk_fp8_f32 v59, v12, v13
	v_cvt_pk_fp8_f32 v60, v16, v17
	v_cvt_pk_fp8_f32 v61, v20, v21
	v_cvt_pk_fp8_f32 v62, v24, v25
	v_cvt_pk_fp8_f32 v63, v28, v29
	v_cvt_pk_fp8_f32 v64, v32, v33
	v_cvt_pk_fp8_f32 v65, v36, v37
	v_cvt_pk_fp8_f32 v58, v10, v11 op_sel:[0,0,1]
	v_cvt_pk_fp8_f32 v59, v14, v15 op_sel:[0,0,1]
	v_cvt_pk_fp8_f32 v60, v18, v19 op_sel:[0,0,1]
	v_cvt_pk_fp8_f32 v61, v22, v23 op_sel:[0,0,1]
	v_cvt_pk_fp8_f32 v62, v26, v27 op_sel:[0,0,1]
	v_cvt_pk_fp8_f32 v63, v30, v31 op_sel:[0,0,1]
	v_cvt_pk_fp8_f32 v64, v34, v35 op_sel:[0,0,1]
	v_cvt_pk_fp8_f32 v65, v38, v39 op_sel:[0,0,1]
	s_lshl_b32 s11, s4, 7
	v_add_u32_e32 v66, s11, v56
	v_add_u32_e32 v67, 0x400000, v66
	v_add_u32_e32 v68, 0x800000, v66
	v_add_u32_e32 v69, 0xc00000, v66
	v_add_u32_e32 v70, 0x1000000, v66
	v_add_u32_e32 v71, 0x1400000, v66
	v_add_u32_e32 v72, 0x1800000, v66
	v_add_u32_e32 v73, 0x1c00000, v66
	global_store_dword v66, v58, s[6:7]
	global_store_dword v67, v59, s[6:7]
	global_store_dword v68, v60, s[6:7]
	global_store_dword v69, v61, s[6:7]
	global_store_dword v70, v62, s[6:7]
	global_store_dword v71, v63, s[6:7]
	global_store_dword v72, v64, s[6:7]
	global_store_dword v73, v65, s[6:7]
	s_add_u32 s4, s4, s10
	s_cmp_ge_u32 s4, 0x4000
	s_cbranch_scc1 .Ldfv_done
	s_add_u32 s11, s4, s10
	s_min_u32 s11, s11, 0x3fff
	s_mov_b32 s101, s11
	s_add_u32 s11, s101, 0x4000
	s_lshl_b32 s11, s11, 13
	v_add_u32_e32 v40, s11, v7
	v_add_u32_e32 v41, 0x1000, v40
	global_load_dwordx4 v[8:11], v40, s[8:9] nt
	global_load_dwordx4 v[12:15], v40, s[8:9] offset:1024 nt
	global_load_dwordx4 v[16:19], v40, s[8:9] offset:2048 nt
	global_load_dwordx4 v[20:23], v40, s[8:9] offset:3072 nt
	global_load_dwordx4 v[24:27], v41, s[8:9] nt
	global_load_dwordx4 v[28:31], v41, s[8:9] offset:1024 nt
	global_load_dwordx4 v[32:35], v41, s[8:9] offset:2048 nt
	global_load_dwordx4 v[36:39], v41, s[8:9] offset:3072 nt
	s_waitcnt vmcnt(8)
	v_max3_f32 v42, |v76|, |v77|, |v78|
	v_max3_f32 v43, |v80|, |v81|, |v82|
	v_max3_f32 v44, |v84|, |v85|, |v86|
	v_max3_f32 v45, |v88|, |v89|, |v90|
	v_max3_f32 v46, |v92|, |v93|, |v94|
	v_max3_f32 v47, |v96|, |v97|, |v98|
	v_max3_f32 v48, |v100|, |v101|, |v102|
	v_max3_f32 v49, |v104|, |v105|, |v106|
	v_max_f32_e64 v42, v42, |v79|
	v_max_f32_e64 v43, v43, |v83|
	v_max_f32_e64 v44, v44, |v87|
	v_max_f32_e64 v45, v45, |v91|
	v_max_f32_e64 v46, v46, |v95|
	v_max_f32_e64 v47, v47, |v99|
	v_max_f32_e64 v48, v48, |v103|
	v_max_f32_e64 v49, v49, |v107|
	v_max3_f32 v42, v42, v43, v44
	v_max3_f32 v45, v45, v46, v47
	v_max3_f32 v42, v42, v45, v48
	v_max_f32_e32 v42, v42, v49
	s_nop 1
	v_max_f32_dpp v43, v42, v42 quad_perm:[1,0,3,2] row_mask:0xf bank_mask:0xf bound_ctrl:1
	s_nop 1
	v_max_f32_dpp v42, v43, v43 quad_perm:[2,3,0,1] row_mask:0xf bank_mask:0xf bound_ctrl:1
	s_nop 1
	v_max_f32_dpp v43, v42, v42 row_half_mirror row_mask:0xf bank_mask:0xf bound_ctrl:1
	s_nop 1
	v_max_f32_dpp v42, v43, v43 row_mirror row_mask:0xf bank_mask:0xf bound_ctrl:1
	s_nop 1
	v_mov_b32_e32 v43, v42
	s_nop 1
	v_permlane16_swap_b32_e32 v42, v43
	v_max_f32_e32 v42, v42, v43
	v_mov_b32_e32 v43, v42
	s_nop 1
	v_permlane32_swap_b32_e32 v42, v43
	v_max_f32_e32 v49, v42, v43
	v_mul_f32_e32 v44, 0x3b124925, v49
	s_add_u32 s11, s4, 0x4000
	s_lshl_b32 s11, s11, 2
	s_add_u32 s11, s11, 0x12a20000
	v_mov_b32_e32 v45, s11
	s_mov_b64 exec, 1
	global_store_dword v45, v44, s[6:7]
	s_mov_b64 exec, -1
	v_mov_b32_e32 v46, 0x43e00000
	v_div_scale_f32 v42, s[100:101], v49, v49, v46
	v_rcp_f32_e32 v43, v42
	s_nop 0
	v_fma_f32 v44, -v42, v43, 1.0
	v_fmac_f32_e32 v43, v44, v43
	v_div_scale_f32 v44, vcc, v46, v49, v46
	v_mul_f32_e32 v45, v44, v43
	v_fma_f32 v47, -v42, v45, v44
	v_fmac_f32_e32 v45, v47, v43
	v_fma_f32 v42, -v42, v45, v44
	s_nop 1
	v_div_fmas_f32 v42, v42, v43, v45
	v_div_fixup_f32 v42, v42, v49, v46
	v_cmp_lt_f32_e32 vcc, 0, v49
	s_nop 1
	v_cndmask_b32_e32 v48, 0, v42, vcc
	v_mul_f32_e32 v76, v76, v48
	v_mul_f32_e32 v77, v77, v48
	v_mul_f32_e32 v78, v78, v48
	v_mul_f32_e32 v79, v79, v48
	v_mul_f32_e32 v80, v80, v48
	v_mul_f32_e32 v81, v81, v48
	v_mul_f32_e32 v82, v82, v48
	v_mul_f32_e32 v83, v83, v48
	v_mul_f32_e32 v84, v84, v48
	v_mul_f32_e32 v85, v85, v48
	v_mul_f32_e32 v86, v86, v48
	v_mul_f32_e32 v87, v87, v48
	v_mul_f32_e32 v88, v88, v48
	v_mul_f32_e32 v89, v89, v48
	v_mul_f32_e32 v90, v90, v48
	v_mul_f32_e32 v91, v91, v48
	v_mul_f32_e32 v92, v92, v48
	v_mul_f32_e32 v93, v93, v48
	v_mul_f32_e32 v94, v94, v48
	v_mul_f32_e32 v95, v95, v48
	v_mul_f32_e32 v96, v96, v48
	v_mul_f32_e32 v97, v97, v48
	v_mul_f32_e32 v98, v98, v48
	v_mul_f32_e32 v99, v99, v48
	v_mul_f32_e32 v100, v100, v48
	v_mul_f32_e32 v101, v101, v48
	v_mul_f32_e32 v102, v102, v48
	v_mul_f32_e32 v103, v103, v48
	v_mul_f32_e32 v104, v104, v48
	v_mul_f32_e32 v105, v105, v48
	v_mul_f32_e32 v106, v106, v48
	v_mul_f32_e32 v107, v107, v48
	v_mov_b32_e32 v58, 0
	v_mov_b32_e32 v59, 0
	v_mov_b32_e32 v60, 0
	v_mov_b32_e32 v61, 0
	v_mov_b32_e32 v62, 0
	v_mov_b32_e32 v63, 0
	v_mov_b32_e32 v64, 0
	v_mov_b32_e32 v65, 0
	v_cvt_pk_fp8_f32 v58, v76, v77
	v_cvt_pk_fp8_f32 v59, v80, v81
	v_cvt_pk_fp8_f32 v60, v84, v85
	v_cvt_pk_fp8_f32 v61, v88, v89
	v_cvt_pk_fp8_f32 v62, v92, v93
	v_cvt_pk_fp8_f32 v63, v96, v97
	v_cvt_pk_fp8_f32 v64, v100, v101
	v_cvt_pk_fp8_f32 v65, v104, v105
	v_cvt_pk_fp8_f32 v58, v78, v79 op_sel:[0,0,1]
	v_cvt_pk_fp8_f32 v59, v82, v83 op_sel:[0,0,1]
	v_cvt_pk_fp8_f32 v60, v86, v87 op_sel:[0,0,1]
	v_cvt_pk_fp8_f32 v61, v90, v91 op_sel:[0,0,1]
	v_cvt_pk_fp8_f32 v62, v94, v95 op_sel:[0,0,1]
	v_cvt_pk_fp8_f32 v63, v98, v99 op_sel:[0,0,1]
	v_cvt_pk_fp8_f32 v64, v102, v103 op_sel:[0,0,1]
	v_cvt_pk_fp8_f32 v65, v106, v107 op_sel:[0,0,1]
	s_lshl_b32 s11, s4, 7
	v_add_u32_e32 v66, s11, v56
	v_add_u32_e32 v67, 0x400000, v66
	v_add_u32_e32 v68, 0x800000, v66
	v_add_u32_e32 v69, 0xc00000, v66
	v_add_u32_e32 v70, 0x1000000, v66
	v_add_u32_e32 v71, 0x1400000, v66
	v_add_u32_e32 v72, 0x1800000, v66
	v_add_u32_e32 v73, 0x1c00000, v66
	global_store_dword v66, v58, s[6:7]
	global_store_dword v67, v59, s[6:7]
	global_store_dword v68, v60, s[6:7]
	global_store_dword v69, v61, s[6:7]
	global_store_dword v70, v62, s[6:7]
	global_store_dword v71, v63, s[6:7]
	global_store_dword v72, v64, s[6:7]
	global_store_dword v73, v65, s[6:7]
	s_add_u32 s4, s4, s10
	s_cmp_ge_u32 s4, 0x4000
	s_cbranch_scc1 .Ldfv_done
	s_branch .Ldfv_loop

.Ldfv_end:
	v_readlane_b32 s4, v255, 36
	s_waitcnt vmcnt(0)
	s_waitcnt lgkmcnt(0)
	s_barrier
	s_mov_b64 s[6:7], exec
	v_readlane_b32 s8, v254, 52
	v_readlane_b32 s9, v254, 53
	v_readlane_b32 s56, v255, 8
	s_and_b64 s[8:9], s[6:7], s[8:9]
	v_readlane_b32 s66, v255, 18
	v_readlane_b32 s67, v255, 19
	v_readlane_b32 s70, v255, 22
	v_readlane_b32 s71, v255, 23
	v_readlane_b32 s83, v255, 30
	v_readlane_b32 s97, v255, 31
	v_readlane_b32 s57, v255, 9
	v_readlane_b32 s58, v255, 10
	v_readlane_b32 s59, v255, 11
	v_readlane_b32 s60, v255, 12
	v_readlane_b32 s61, v255, 13
	v_readlane_b32 s62, v255, 14
	v_readlane_b32 s63, v255, 15
	v_readlane_b32 s64, v255, 16
	v_readlane_b32 s65, v255, 17
	v_readlane_b32 s68, v255, 20
	v_readlane_b32 s69, v255, 21
	s_mov_b64 exec, s[8:9]
	s_cbranch_execz .LBB0_759
	v_readlane_b32 s8, v252, 42
	s_waitcnt vmcnt(0) expcnt(0) lgkmcnt(0)
	s_nop 0
	v_mov_b32_e32 v2, s8
	ds_read_b32 v5, v2
	ds_read_b32 v2, v2 offset:4
	s_waitcnt lgkmcnt(1)
	v_cmp_ne_u32_e32 vcc, 0, v5
	s_cbranch_vccnz .LBB0_727
	v_readlane_b32 s10, v252, 4
	v_readlane_b32 s11, v252, 5
	s_load_dwordx2 s[8:9], s[10:11], 0x4
	s_mov_b32 s15, 1
	s_waitcnt lgkmcnt(0)
	s_mul_i32 s14, s8, s82
	s_mul_i32 s14, s14, s9
	s_branch .LBB0_714

	.amdhsa_kernel _Z6mk_fwd4Args
		.amdhsa_group_segment_fixed_size 0
		.amdhsa_private_segment_fixed_size 0
		.amdhsa_kernarg_size 464
		.amdhsa_user_sgpr_count 2
		.amdhsa_user_sgpr_dispatch_ptr 0
		.amdhsa_user_sgpr_queue_ptr 0
		.amdhsa_user_sgpr_kernarg_segment_ptr 1
		.amdhsa_user_sgpr_dispatch_id 0
		.amdhsa_user_sgpr_kernarg_preload_length 0
		.amdhsa_user_sgpr_kernarg_preload_offset 0
		.amdhsa_user_sgpr_private_segment_size 0
		.amdhsa_uses_dynamic_stack 0
		.amdhsa_enable_private_segment 0
		.amdhsa_system_sgpr_workgroup_id_x 1
		.amdhsa_system_sgpr_workgroup_id_y 0
		.amdhsa_system_sgpr_workgroup_id_z 0
		.amdhsa_system_sgpr_workgroup_info 0
		.amdhsa_system_vgpr_workitem_id 0
		.amdhsa_next_free_vgpr 256
		.amdhsa_next_free_sgpr 102
		.amdhsa_accum_offset 256
		.amdhsa_reserve_vcc 1
		.amdhsa_float_round_mode_32 0
		.amdhsa_float_round_mode_16_64 0
		.amdhsa_float_denorm_mode_32 3
		.amdhsa_float_denorm_mode_16_64 3
		.amdhsa_dx10_clamp 1
		.amdhsa_ieee_mode 1
		.amdhsa_fp16_overflow 0
		.amdhsa_tg_split 0
		.amdhsa_exception_fp_ieee_invalid_op 0
		.amdhsa_exception_fp_denorm_src 0
		.amdhsa_exception_fp_ieee_div_zero 0
		.amdhsa_exception_fp_ieee_overflow 0
		.amdhsa_exception_fp_ieee_underflow 0
		.amdhsa_exception_fp_ieee_inexact 0
		.amdhsa_exception_int_div_zero 0
	.end_amdhsa_kernel

amdhsa.kernels:
  - .agpr_count:     0
    .args:
      - .offset:         0
        .size:           208
        .value_kind:     by_value
      - .offset:         208
        .size:           4
        .value_kind:     hidden_block_count_x
      - .offset:         212
        .size:           4
        .value_kind:     hidden_block_count_y
      - .offset:         216
        .size:           4
        .value_kind:     hidden_block_count_z
      - .offset:         220
        .size:           2
        .value_kind:     hidden_group_size_x
      - .offset:         222
        .size:           2
        .value_kind:     hidden_group_size_y
      - .offset:         224
        .size:           2
        .value_kind:     hidden_group_size_z
      - .offset:         226
        .size:           2
        .value_kind:     hidden_remainder_x
      - .offset:         228
        .size:           2
        .value_kind:     hidden_remainder_y
      - .offset:         230
        .size:           2
        .value_kind:     hidden_remainder_z
      - .offset:         248
        .size:           8
        .value_kind:     hidden_global_offset_x
      - .offset:         256
        .size:           8
        .value_kind:     hidden_global_offset_y
      - .offset:         264
        .size:           8
        .value_kind:     hidden_global_offset_z
      - .offset:         272
        .size:           2
        .value_kind:     hidden_grid_dims
      - .offset:         328
        .size:           4
        .value_kind:     hidden_dynamic_lds_size
    .group_segment_fixed_size: 0
    .kernarg_segment_align: 8
    .kernarg_segment_size: 464
    .language:       OpenCL C
    .language_version:
      - 2
      - 0
    .max_flat_workgroup_size: 512
    .name:           _Z6mk_fwd4Args
    .private_segment_fixed_size: 0
    .sgpr_count:     108
    .sgpr_spill_count: 277
    .symbol:         _Z6mk_fwd4Args.kd
    .uniform_work_group_size: 1
    .uses_dynamic_stack: false
    .vgpr_count:     256
    .vgpr_spill_count: 0
    .wavefront_size: 64
